# baseline (speedup 1.0000x reference)
.LBB3_11:
	s_lshl_b32 s58, s42, 7
	s_add_i32 s59, s41, 0x400
	s_lshr_b32 s59, s59, 6
	s_bfe_u32 s60, s20, 0x1000c
	s_add_i32 s59, s59, s60
	s_lshl_b32 s59, s59, 19
	s_add_u32 s58, s58, s59
	s_add_u32 s58, s56, s58
	s_addc_u32 s59, s57, 0
	s_add_u32 s60, s58, 0x4000
	s_addc_u32 s61, s59, 0
	s_add_u32 s62, s58, 0x100000
	s_addc_u32 s63, s59, 0
	s_add_u32 s64, s62, 0x4000
	s_addc_u32 s65, s63, 0
	s_lshr_b32 s66, s41, 7
	s_bfe_u32 s67, s20, 0x1000c
	s_add_i32 s66, s66, s67
	s_lshl_b32 s66, s66, 14
	s_lshl_b32 s67, s42, 2
	s_add_u32 s66, s66, s67
	s_add_u32 s66, s14, s66
	s_addc_u32 s67, s15, 0
	v_add_u32_e32 v172, s43, v207
	v_pk_fma_f32 v[244:245], v[244:245], -0.5, -0.5 op_sel_hi:[1,0,0]
	v_pk_fma_f32 v[246:247], v[246:247], -0.5, -0.5 op_sel_hi:[1,0,0]
	v_pk_fma_f32 v[248:249], v[248:249], -0.5, -0.5 op_sel_hi:[1,0,0]
	v_pk_fma_f32 v[250:251], v[250:251], -0.5, -0.5 op_sel_hi:[1,0,0]
	v_pk_fma_f32 v[252:253], v[252:253], -0.5, -0.5 op_sel_hi:[1,0,0]
	v_pk_fma_f32 v[254:255], v[254:255], -0.5, -0.5 op_sel_hi:[1,0,0]
	v_pk_fma_f32 v[232:233], v[232:233], -0.5, -0.5 op_sel_hi:[1,0,0]
	v_pk_fma_f32 v[234:235], v[234:235], -0.5, -0.5 op_sel_hi:[1,0,0]
	v_pk_mul_f32 v[134:135], v[244:245], v[246:247]
	v_pk_mul_f32 v[146:147], v[248:249], v[250:251]
	v_pk_mul_f32 v[180:181], v[252:253], v[254:255]
	v_pk_mul_f32 v[236:237], v[232:233], v[234:235]
	v_mul_f32_e32 v188, v134, v135
	v_mul_f32_e32 v190, v146, v147
	v_mul_f32_e32 v189, v180, v181
	v_mul_f32_e32 v191, v236, v237
	v_pk_mul_f32 v[192:193], v[188:189], v[190:191]
	v_mul_f32_e32 v162, v192, v193
	v_rcp_f32_e32 v173, v162
	v_pk_add_f32 v[164:165], v[114:115], v[116:117]
	v_pk_add_f32 v[164:165], v[164:165], v[78:79]
	v_pk_add_f32 v[164:165], v[164:165], v[80:81]
	v_pk_add_f32 v[164:165], v[164:165], v[106:107]
	v_pk_add_f32 v[164:165], v[164:165], v[108:109]
	v_pk_add_f32 v[164:165], v[164:165], v[70:71]
	v_pk_add_f32 v[164:165], v[164:165], v[72:73]
	v_pk_mul_f32 v[230:231], v[172:173], v[192:193] op_sel:[1,1] op_sel_hi:[1,0]
	v_pk_mul_f32 v[192:193], v[230:231], v[190:191]
	v_pk_mul_f32 v[190:191], v[230:231], v[188:189]
	v_pk_mul_f32 v[136:137], v[192:193], v[134:135] op_sel:[0,1] op_sel_hi:[0,0]
	v_pk_mul_f32 v[148:149], v[190:191], v[146:147] op_sel:[0,1] op_sel_hi:[0,0]
	v_pk_mul_f32 v[182:183], v[192:193], v[180:181] op_sel:[1,1] op_sel_hi:[1,0]
	v_pk_mul_f32 v[238:239], v[190:191], v[236:237] op_sel:[1,1] op_sel_hi:[1,0]
	v_pk_fma_f32 v[138:139], v[136:137], v[246:247], 1.0 op_sel_hi:[1,1,0]
	v_pk_fma_f32 v[140:141], v[136:137], v[244:245], 1.0 op_sel_hi:[1,1,0]
	v_pk_fma_f32 v[150:151], v[148:149], v[250:251], 1.0 op_sel_hi:[1,1,0]
	v_pk_fma_f32 v[152:153], v[148:149], v[248:249], 1.0 op_sel_hi:[1,1,0]
	v_pk_fma_f32 v[184:185], v[182:183], v[254:255], 1.0 op_sel_hi:[1,1,0]
	v_pk_fma_f32 v[186:187], v[182:183], v[252:253], 1.0 op_sel_hi:[1,1,0]
	v_pk_fma_f32 v[240:241], v[238:239], v[234:235], 1.0 op_sel_hi:[1,1,0]
	v_pk_fma_f32 v[242:243], v[238:239], v[232:233], 1.0 op_sel_hi:[1,1,0]
	v_cvt_pk_bf16_f32 v154, v138, v139
	v_cvt_pk_bf16_f32 v155, v140, v141
	v_cvt_pk_bf16_f32 v156, v150, v151
	v_cvt_pk_bf16_f32 v157, v152, v153
	v_cvt_pk_bf16_f32 v158, v184, v185
	v_cvt_pk_bf16_f32 v159, v186, v187
	v_cvt_pk_bf16_f32 v160, v240, v241
	v_cvt_pk_bf16_f32 v161, v242, v243
	ds_read_b128 v[114:117], v172
	ds_read_b128 v[78:81], v172 offset:64
	ds_read_b128 v[106:109], v172 offset:128
	ds_read_b128 v[70:73], v172 offset:192
	v_permlane16_swap_b32_e32 v154, v156
	v_permlane16_swap_b32_e32 v155, v157
	global_store_dwordx4 v228, v[154:157], s[58:59] nt
	s_bitcmp1_b32 s20, 12
	s_cbranch_scc1 .Lg1_noX
	s_barrier
	s_setprio 1
